# LN1 router loop unrolled with 4-deep operand ring (was double-buffered) + layer-0 forget-logit loop ring; without the LN2/MoE2 table reuse
# baseline (speedup 1.0000x reference)
.LBB0_3237:
	s_waitcnt vmcnt(0)
	s_add_i32 s10, s8, 0
	s_and_b32 s10, s10, 15
	s_lshl_b32 s64, s10, 6
	v_lshl_add_u64 v[76:77], v[32:33], 0, s[64:65]
	v_lshl_add_u64 v[78:79], v[34:35], 0, s[64:65]
	s_mul_i32 s64, s10, 0xc00
	v_lshl_add_u64 v[80:81], v[36:37], 0, s[64:65]
	global_load_dwordx4 v[56:59], v[76:77], off
	global_load_dwordx4 v[60:63], v[78:79], off
	global_load_dwordx4 v[88:91], v[80:81], off
	global_load_dwordx4 v[92:95], v[80:81], off offset:1024
	global_load_dwordx4 v[96:99], v[80:81], off offset:2048
	s_add_i32 s10, s8, 1
	s_and_b32 s10, s10, 15
	s_lshl_b32 s64, s10, 6
	v_lshl_add_u64 v[76:77], v[32:33], 0, s[64:65]
	v_lshl_add_u64 v[78:79], v[34:35], 0, s[64:65]
	s_mul_i32 s64, s10, 0xc00
	v_lshl_add_u64 v[80:81], v[36:37], 0, s[64:65]
	global_load_dwordx4 v[68:71], v[76:77], off
	global_load_dwordx4 v[72:75], v[78:79], off
	global_load_dwordx4 v[100:103], v[80:81], off
	global_load_dwordx4 v[104:107], v[80:81], off offset:1024
	global_load_dwordx4 v[108:111], v[80:81], off offset:2048
	s_add_i32 s10, s8, 2
	s_and_b32 s10, s10, 15
	s_lshl_b32 s64, s10, 6
	v_lshl_add_u64 v[76:77], v[32:33], 0, s[64:65]
	v_lshl_add_u64 v[78:79], v[34:35], 0, s[64:65]
	s_mul_i32 s64, s10, 0xc00
	v_lshl_add_u64 v[80:81], v[36:37], 0, s[64:65]
	global_load_dwordx4 v[112:115], v[76:77], off
	global_load_dwordx4 v[116:119], v[78:79], off
	global_load_dwordx4 v[120:123], v[80:81], off
	global_load_dwordx4 v[124:127], v[80:81], off offset:1024
	global_load_dwordx4 v[128:131], v[80:81], off offset:2048
	s_add_i32 s10, s8, 3
	s_and_b32 s10, s10, 15
	s_lshl_b32 s64, s10, 6
	v_lshl_add_u64 v[76:77], v[32:33], 0, s[64:65]
	v_lshl_add_u64 v[78:79], v[34:35], 0, s[64:65]
	s_mul_i32 s64, s10, 0xc00
	v_lshl_add_u64 v[80:81], v[36:37], 0, s[64:65]
	global_load_dwordx4 v[132:135], v[76:77], off
	global_load_dwordx4 v[136:139], v[78:79], off
	global_load_dwordx4 v[140:143], v[80:81], off
	global_load_dwordx4 v[144:147], v[80:81], off offset:1024
	global_load_dwordx4 v[148:151], v[80:81], off offset:2048
	s_waitcnt vmcnt(15)
	v_mfma_f32_16x16x4_f32 v[14:17], v56, v88, v[14:17]
	v_mfma_f32_16x16x4_f32 v[6:9], v60, v88, v[6:9]
	v_mfma_f32_16x16x4_f32 v[14:17], v57, v89, v[14:17]
	v_mfma_f32_16x16x4_f32 v[6:9], v61, v89, v[6:9]
	v_mfma_f32_16x16x4_f32 v[14:17], v58, v90, v[14:17]
	v_mfma_f32_16x16x4_f32 v[6:9], v62, v90, v[6:9]
	v_mfma_f32_16x16x4_f32 v[14:17], v59, v91, v[14:17]
	v_mfma_f32_16x16x4_f32 v[6:9], v63, v91, v[6:9]
	v_mfma_f32_16x16x4_f32 v[10:13], v56, v92, v[10:13]
	v_mfma_f32_16x16x4_f32 v[2:5], v60, v92, v[2:5]
	v_mfma_f32_16x16x4_f32 v[10:13], v57, v93, v[10:13]
	v_mfma_f32_16x16x4_f32 v[2:5], v61, v93, v[2:5]
	v_mfma_f32_16x16x4_f32 v[10:13], v58, v94, v[10:13]
	v_mfma_f32_16x16x4_f32 v[2:5], v62, v94, v[2:5]
	v_mfma_f32_16x16x4_f32 v[10:13], v59, v95, v[10:13]
	v_mfma_f32_16x16x4_f32 v[2:5], v63, v95, v[2:5]
	v_mfma_f32_16x16x4_f32 v[22:25], v56, v96, v[22:25]
	v_mfma_f32_16x16x4_f32 v[18:21], v60, v96, v[18:21]
	v_mfma_f32_16x16x4_f32 v[22:25], v57, v97, v[22:25]
	v_mfma_f32_16x16x4_f32 v[18:21], v61, v97, v[18:21]
	v_mfma_f32_16x16x4_f32 v[22:25], v58, v98, v[22:25]
	v_mfma_f32_16x16x4_f32 v[18:21], v62, v98, v[18:21]
	v_mfma_f32_16x16x4_f32 v[22:25], v59, v99, v[22:25]
	v_mfma_f32_16x16x4_f32 v[18:21], v63, v99, v[18:21]
	s_add_i32 s10, s8, 4
	s_and_b32 s10, s10, 15
	s_lshl_b32 s64, s10, 6
	v_lshl_add_u64 v[76:77], v[32:33], 0, s[64:65]
	v_lshl_add_u64 v[78:79], v[34:35], 0, s[64:65]
	s_mul_i32 s64, s10, 0xc00
	v_lshl_add_u64 v[80:81], v[36:37], 0, s[64:65]
	global_load_dwordx4 v[56:59], v[76:77], off
	global_load_dwordx4 v[60:63], v[78:79], off
	global_load_dwordx4 v[88:91], v[80:81], off
	global_load_dwordx4 v[92:95], v[80:81], off offset:1024
	global_load_dwordx4 v[96:99], v[80:81], off offset:2048
	s_waitcnt vmcnt(15)
	v_mfma_f32_16x16x4_f32 v[14:17], v68, v100, v[14:17]
	v_mfma_f32_16x16x4_f32 v[6:9], v72, v100, v[6:9]
	v_mfma_f32_16x16x4_f32 v[14:17], v69, v101, v[14:17]
	v_mfma_f32_16x16x4_f32 v[6:9], v73, v101, v[6:9]
	v_mfma_f32_16x16x4_f32 v[14:17], v70, v102, v[14:17]
	v_mfma_f32_16x16x4_f32 v[6:9], v74, v102, v[6:9]
	v_mfma_f32_16x16x4_f32 v[14:17], v71, v103, v[14:17]
	v_mfma_f32_16x16x4_f32 v[6:9], v75, v103, v[6:9]
	v_mfma_f32_16x16x4_f32 v[10:13], v68, v104, v[10:13]
	v_mfma_f32_16x16x4_f32 v[2:5], v72, v104, v[2:5]
	v_mfma_f32_16x16x4_f32 v[10:13], v69, v105, v[10:13]
	v_mfma_f32_16x16x4_f32 v[2:5], v73, v105, v[2:5]
	v_mfma_f32_16x16x4_f32 v[10:13], v70, v106, v[10:13]
	v_mfma_f32_16x16x4_f32 v[2:5], v74, v106, v[2:5]
	v_mfma_f32_16x16x4_f32 v[10:13], v71, v107, v[10:13]
	v_mfma_f32_16x16x4_f32 v[2:5], v75, v107, v[2:5]
	v_mfma_f32_16x16x4_f32 v[22:25], v68, v108, v[22:25]
	v_mfma_f32_16x16x4_f32 v[18:21], v72, v108, v[18:21]
	v_mfma_f32_16x16x4_f32 v[22:25], v69, v109, v[22:25]
	v_mfma_f32_16x16x4_f32 v[18:21], v73, v109, v[18:21]
	v_mfma_f32_16x16x4_f32 v[22:25], v70, v110, v[22:25]
	v_mfma_f32_16x16x4_f32 v[18:21], v74, v110, v[18:21]
	v_mfma_f32_16x16x4_f32 v[22:25], v71, v111, v[22:25]
	v_mfma_f32_16x16x4_f32 v[18:21], v75, v111, v[18:21]
	s_add_i32 s10, s8, 5
	s_and_b32 s10, s10, 15
	s_lshl_b32 s64, s10, 6
	v_lshl_add_u64 v[76:77], v[32:33], 0, s[64:65]
	v_lshl_add_u64 v[78:79], v[34:35], 0, s[64:65]
	s_mul_i32 s64, s10, 0xc00
	v_lshl_add_u64 v[80:81], v[36:37], 0, s[64:65]
	global_load_dwordx4 v[68:71], v[76:77], off
	global_load_dwordx4 v[72:75], v[78:79], off
	global_load_dwordx4 v[100:103], v[80:81], off
	global_load_dwordx4 v[104:107], v[80:81], off offset:1024
	global_load_dwordx4 v[108:111], v[80:81], off offset:2048
	s_waitcnt vmcnt(15)
	v_mfma_f32_16x16x4_f32 v[14:17], v112, v120, v[14:17]
	v_mfma_f32_16x16x4_f32 v[6:9], v116, v120, v[6:9]
	v_mfma_f32_16x16x4_f32 v[14:17], v113, v121, v[14:17]
	v_mfma_f32_16x16x4_f32 v[6:9], v117, v121, v[6:9]
	v_mfma_f32_16x16x4_f32 v[14:17], v114, v122, v[14:17]
	v_mfma_f32_16x16x4_f32 v[6:9], v118, v122, v[6:9]
	v_mfma_f32_16x16x4_f32 v[14:17], v115, v123, v[14:17]
	v_mfma_f32_16x16x4_f32 v[6:9], v119, v123, v[6:9]
	v_mfma_f32_16x16x4_f32 v[10:13], v112, v124, v[10:13]
	v_mfma_f32_16x16x4_f32 v[2:5], v116, v124, v[2:5]
	v_mfma_f32_16x16x4_f32 v[10:13], v113, v125, v[10:13]
	v_mfma_f32_16x16x4_f32 v[2:5], v117, v125, v[2:5]
	v_mfma_f32_16x16x4_f32 v[10:13], v114, v126, v[10:13]
	v_mfma_f32_16x16x4_f32 v[2:5], v118, v126, v[2:5]
	v_mfma_f32_16x16x4_f32 v[10:13], v115, v127, v[10:13]
	v_mfma_f32_16x16x4_f32 v[2:5], v119, v127, v[2:5]
	v_mfma_f32_16x16x4_f32 v[22:25], v112, v128, v[22:25]
	v_mfma_f32_16x16x4_f32 v[18:21], v116, v128, v[18:21]
	v_mfma_f32_16x16x4_f32 v[22:25], v113, v129, v[22:25]
	v_mfma_f32_16x16x4_f32 v[18:21], v117, v129, v[18:21]
	v_mfma_f32_16x16x4_f32 v[22:25], v114, v130, v[22:25]
	v_mfma_f32_16x16x4_f32 v[18:21], v118, v130, v[18:21]
	v_mfma_f32_16x16x4_f32 v[22:25], v115, v131, v[22:25]
	v_mfma_f32_16x16x4_f32 v[18:21], v119, v131, v[18:21]
	s_add_i32 s10, s8, 6
	s_and_b32 s10, s10, 15
	s_lshl_b32 s64, s10, 6
	v_lshl_add_u64 v[76:77], v[32:33], 0, s[64:65]
	v_lshl_add_u64 v[78:79], v[34:35], 0, s[64:65]
	s_mul_i32 s64, s10, 0xc00
	v_lshl_add_u64 v[80:81], v[36:37], 0, s[64:65]
	global_load_dwordx4 v[112:115], v[76:77], off
	global_load_dwordx4 v[116:119], v[78:79], off
	global_load_dwordx4 v[120:123], v[80:81], off
	global_load_dwordx4 v[124:127], v[80:81], off offset:1024
	global_load_dwordx4 v[128:131], v[80:81], off offset:2048
	s_waitcnt vmcnt(15)
	v_mfma_f32_16x16x4_f32 v[14:17], v132, v140, v[14:17]
	v_mfma_f32_16x16x4_f32 v[6:9], v136, v140, v[6:9]
	v_mfma_f32_16x16x4_f32 v[14:17], v133, v141, v[14:17]
	v_mfma_f32_16x16x4_f32 v[6:9], v137, v141, v[6:9]
	v_mfma_f32_16x16x4_f32 v[14:17], v134, v142, v[14:17]
	v_mfma_f32_16x16x4_f32 v[6:9], v138, v142, v[6:9]
	v_mfma_f32_16x16x4_f32 v[14:17], v135, v143, v[14:17]
	v_mfma_f32_16x16x4_f32 v[6:9], v139, v143, v[6:9]
	v_mfma_f32_16x16x4_f32 v[10:13], v132, v144, v[10:13]
	v_mfma_f32_16x16x4_f32 v[2:5], v136, v144, v[2:5]
	v_mfma_f32_16x16x4_f32 v[10:13], v133, v145, v[10:13]
	v_mfma_f32_16x16x4_f32 v[2:5], v137, v145, v[2:5]
	v_mfma_f32_16x16x4_f32 v[10:13], v134, v146, v[10:13]
	v_mfma_f32_16x16x4_f32 v[2:5], v138, v146, v[2:5]
	v_mfma_f32_16x16x4_f32 v[10:13], v135, v147, v[10:13]
	v_mfma_f32_16x16x4_f32 v[2:5], v139, v147, v[2:5]
	v_mfma_f32_16x16x4_f32 v[22:25], v132, v148, v[22:25]
	v_mfma_f32_16x16x4_f32 v[18:21], v136, v148, v[18:21]
	v_mfma_f32_16x16x4_f32 v[22:25], v133, v149, v[22:25]
	v_mfma_f32_16x16x4_f32 v[18:21], v137, v149, v[18:21]
	v_mfma_f32_16x16x4_f32 v[22:25], v134, v150, v[22:25]
	v_mfma_f32_16x16x4_f32 v[18:21], v138, v150, v[18:21]
	v_mfma_f32_16x16x4_f32 v[22:25], v135, v151, v[22:25]
	v_mfma_f32_16x16x4_f32 v[18:21], v139, v151, v[18:21]
	s_add_i32 s10, s8, 7
	s_and_b32 s10, s10, 15
	s_lshl_b32 s64, s10, 6
	v_lshl_add_u64 v[76:77], v[32:33], 0, s[64:65]
	v_lshl_add_u64 v[78:79], v[34:35], 0, s[64:65]
	s_mul_i32 s64, s10, 0xc00
	v_lshl_add_u64 v[80:81], v[36:37], 0, s[64:65]
	global_load_dwordx4 v[132:135], v[76:77], off
	global_load_dwordx4 v[136:139], v[78:79], off
	global_load_dwordx4 v[140:143], v[80:81], off
	global_load_dwordx4 v[144:147], v[80:81], off offset:1024
	global_load_dwordx4 v[148:151], v[80:81], off offset:2048
	s_waitcnt vmcnt(15)
	v_mfma_f32_16x16x4_f32 v[14:17], v56, v88, v[14:17]
	v_mfma_f32_16x16x4_f32 v[6:9], v60, v88, v[6:9]
	v_mfma_f32_16x16x4_f32 v[14:17], v57, v89, v[14:17]
	v_mfma_f32_16x16x4_f32 v[6:9], v61, v89, v[6:9]
	v_mfma_f32_16x16x4_f32 v[14:17], v58, v90, v[14:17]
	v_mfma_f32_16x16x4_f32 v[6:9], v62, v90, v[6:9]
	v_mfma_f32_16x16x4_f32 v[14:17], v59, v91, v[14:17]
	v_mfma_f32_16x16x4_f32 v[6:9], v63, v91, v[6:9]
	v_mfma_f32_16x16x4_f32 v[10:13], v56, v92, v[10:13]
	v_mfma_f32_16x16x4_f32 v[2:5], v60, v92, v[2:5]
	v_mfma_f32_16x16x4_f32 v[10:13], v57, v93, v[10:13]
	v_mfma_f32_16x16x4_f32 v[2:5], v61, v93, v[2:5]
	v_mfma_f32_16x16x4_f32 v[10:13], v58, v94, v[10:13]
	v_mfma_f32_16x16x4_f32 v[2:5], v62, v94, v[2:5]
	v_mfma_f32_16x16x4_f32 v[10:13], v59, v95, v[10:13]
	v_mfma_f32_16x16x4_f32 v[2:5], v63, v95, v[2:5]
	v_mfma_f32_16x16x4_f32 v[22:25], v56, v96, v[22:25]
	v_mfma_f32_16x16x4_f32 v[18:21], v60, v96, v[18:21]
	v_mfma_f32_16x16x4_f32 v[22:25], v57, v97, v[22:25]
	v_mfma_f32_16x16x4_f32 v[18:21], v61, v97, v[18:21]
	v_mfma_f32_16x16x4_f32 v[22:25], v58, v98, v[22:25]
	v_mfma_f32_16x16x4_f32 v[18:21], v62, v98, v[18:21]
	v_mfma_f32_16x16x4_f32 v[22:25], v59, v99, v[22:25]
	v_mfma_f32_16x16x4_f32 v[18:21], v63, v99, v[18:21]
	s_add_i32 s10, s8, 8
	s_and_b32 s10, s10, 15
	s_lshl_b32 s64, s10, 6
	v_lshl_add_u64 v[76:77], v[32:33], 0, s[64:65]
	v_lshl_add_u64 v[78:79], v[34:35], 0, s[64:65]
	s_mul_i32 s64, s10, 0xc00
	v_lshl_add_u64 v[80:81], v[36:37], 0, s[64:65]
	global_load_dwordx4 v[56:59], v[76:77], off
	global_load_dwordx4 v[60:63], v[78:79], off
	global_load_dwordx4 v[88:91], v[80:81], off
	global_load_dwordx4 v[92:95], v[80:81], off offset:1024
	global_load_dwordx4 v[96:99], v[80:81], off offset:2048
	s_waitcnt vmcnt(15)
	v_mfma_f32_16x16x4_f32 v[14:17], v68, v100, v[14:17]
	v_mfma_f32_16x16x4_f32 v[6:9], v72, v100, v[6:9]
	v_mfma_f32_16x16x4_f32 v[14:17], v69, v101, v[14:17]
	v_mfma_f32_16x16x4_f32 v[6:9], v73, v101, v[6:9]
	v_mfma_f32_16x16x4_f32 v[14:17], v70, v102, v[14:17]
	v_mfma_f32_16x16x4_f32 v[6:9], v74, v102, v[6:9]
	v_mfma_f32_16x16x4_f32 v[14:17], v71, v103, v[14:17]
	v_mfma_f32_16x16x4_f32 v[6:9], v75, v103, v[6:9]
	v_mfma_f32_16x16x4_f32 v[10:13], v68, v104, v[10:13]
	v_mfma_f32_16x16x4_f32 v[2:5], v72, v104, v[2:5]
	v_mfma_f32_16x16x4_f32 v[10:13], v69, v105, v[10:13]
	v_mfma_f32_16x16x4_f32 v[2:5], v73, v105, v[2:5]
	v_mfma_f32_16x16x4_f32 v[10:13], v70, v106, v[10:13]
	v_mfma_f32_16x16x4_f32 v[2:5], v74, v106, v[2:5]
	v_mfma_f32_16x16x4_f32 v[10:13], v71, v107, v[10:13]
	v_mfma_f32_16x16x4_f32 v[2:5], v75, v107, v[2:5]
	v_mfma_f32_16x16x4_f32 v[22:25], v68, v108, v[22:25]
	v_mfma_f32_16x16x4_f32 v[18:21], v72, v108, v[18:21]
	v_mfma_f32_16x16x4_f32 v[22:25], v69, v109, v[22:25]
	v_mfma_f32_16x16x4_f32 v[18:21], v73, v109, v[18:21]
	v_mfma_f32_16x16x4_f32 v[22:25], v70, v110, v[22:25]
	v_mfma_f32_16x16x4_f32 v[18:21], v74, v110, v[18:21]
	v_mfma_f32_16x16x4_f32 v[22:25], v71, v111, v[22:25]
	v_mfma_f32_16x16x4_f32 v[18:21], v75, v111, v[18:21]
	s_add_i32 s10, s8, 9
	s_and_b32 s10, s10, 15
	s_lshl_b32 s64, s10, 6
	v_lshl_add_u64 v[76:77], v[32:33], 0, s[64:65]
	v_lshl_add_u64 v[78:79], v[34:35], 0, s[64:65]
	s_mul_i32 s64, s10, 0xc00
	v_lshl_add_u64 v[80:81], v[36:37], 0, s[64:65]
	global_load_dwordx4 v[68:71], v[76:77], off
	global_load_dwordx4 v[72:75], v[78:79], off
	global_load_dwordx4 v[100:103], v[80:81], off
	global_load_dwordx4 v[104:107], v[80:81], off offset:1024
	global_load_dwordx4 v[108:111], v[80:81], off offset:2048
	s_waitcnt vmcnt(15)
	v_mfma_f32_16x16x4_f32 v[14:17], v112, v120, v[14:17]
	v_mfma_f32_16x16x4_f32 v[6:9], v116, v120, v[6:9]
	v_mfma_f32_16x16x4_f32 v[14:17], v113, v121, v[14:17]
	v_mfma_f32_16x16x4_f32 v[6:9], v117, v121, v[6:9]
	v_mfma_f32_16x16x4_f32 v[14:17], v114, v122, v[14:17]
	v_mfma_f32_16x16x4_f32 v[6:9], v118, v122, v[6:9]
	v_mfma_f32_16x16x4_f32 v[14:17], v115, v123, v[14:17]
	v_mfma_f32_16x16x4_f32 v[6:9], v119, v123, v[6:9]
	v_mfma_f32_16x16x4_f32 v[10:13], v112, v124, v[10:13]
	v_mfma_f32_16x16x4_f32 v[2:5], v116, v124, v[2:5]
	v_mfma_f32_16x16x4_f32 v[10:13], v113, v125, v[10:13]
	v_mfma_f32_16x16x4_f32 v[2:5], v117, v125, v[2:5]
	v_mfma_f32_16x16x4_f32 v[10:13], v114, v126, v[10:13]
	v_mfma_f32_16x16x4_f32 v[2:5], v118, v126, v[2:5]
	v_mfma_f32_16x16x4_f32 v[10:13], v115, v127, v[10:13]
	v_mfma_f32_16x16x4_f32 v[2:5], v119, v127, v[2:5]
	v_mfma_f32_16x16x4_f32 v[22:25], v112, v128, v[22:25]
	v_mfma_f32_16x16x4_f32 v[18:21], v116, v128, v[18:21]
	v_mfma_f32_16x16x4_f32 v[22:25], v113, v129, v[22:25]
	v_mfma_f32_16x16x4_f32 v[18:21], v117, v129, v[18:21]
	v_mfma_f32_16x16x4_f32 v[22:25], v114, v130, v[22:25]
	v_mfma_f32_16x16x4_f32 v[18:21], v118, v130, v[18:21]
	v_mfma_f32_16x16x4_f32 v[22:25], v115, v131, v[22:25]
	v_mfma_f32_16x16x4_f32 v[18:21], v119, v131, v[18:21]
	s_add_i32 s10, s8, 10
	s_and_b32 s10, s10, 15
	s_lshl_b32 s64, s10, 6
	v_lshl_add_u64 v[76:77], v[32:33], 0, s[64:65]
	v_lshl_add_u64 v[78:79], v[34:35], 0, s[64:65]
	s_mul_i32 s64, s10, 0xc00
	v_lshl_add_u64 v[80:81], v[36:37], 0, s[64:65]
	global_load_dwordx4 v[112:115], v[76:77], off
	global_load_dwordx4 v[116:119], v[78:79], off
	global_load_dwordx4 v[120:123], v[80:81], off
	global_load_dwordx4 v[124:127], v[80:81], off offset:1024
	global_load_dwordx4 v[128:131], v[80:81], off offset:2048
	s_waitcnt vmcnt(15)
	v_mfma_f32_16x16x4_f32 v[14:17], v132, v140, v[14:17]
	v_mfma_f32_16x16x4_f32 v[6:9], v136, v140, v[6:9]
	v_mfma_f32_16x16x4_f32 v[14:17], v133, v141, v[14:17]
	v_mfma_f32_16x16x4_f32 v[6:9], v137, v141, v[6:9]
	v_mfma_f32_16x16x4_f32 v[14:17], v134, v142, v[14:17]
	v_mfma_f32_16x16x4_f32 v[6:9], v138, v142, v[6:9]
	v_mfma_f32_16x16x4_f32 v[14:17], v135, v143, v[14:17]
	v_mfma_f32_16x16x4_f32 v[6:9], v139, v143, v[6:9]
	v_mfma_f32_16x16x4_f32 v[10:13], v132, v144, v[10:13]
	v_mfma_f32_16x16x4_f32 v[2:5], v136, v144, v[2:5]
	v_mfma_f32_16x16x4_f32 v[10:13], v133, v145, v[10:13]
	v_mfma_f32_16x16x4_f32 v[2:5], v137, v145, v[2:5]
	v_mfma_f32_16x16x4_f32 v[10:13], v134, v146, v[10:13]
	v_mfma_f32_16x16x4_f32 v[2:5], v138, v146, v[2:5]
	v_mfma_f32_16x16x4_f32 v[10:13], v135, v147, v[10:13]
	v_mfma_f32_16x16x4_f32 v[2:5], v139, v147, v[2:5]
	v_mfma_f32_16x16x4_f32 v[22:25], v132, v148, v[22:25]
	v_mfma_f32_16x16x4_f32 v[18:21], v136, v148, v[18:21]
	v_mfma_f32_16x16x4_f32 v[22:25], v133, v149, v[22:25]
	v_mfma_f32_16x16x4_f32 v[18:21], v137, v149, v[18:21]
	v_mfma_f32_16x16x4_f32 v[22:25], v134, v150, v[22:25]
	v_mfma_f32_16x16x4_f32 v[18:21], v138, v150, v[18:21]
	v_mfma_f32_16x16x4_f32 v[22:25], v135, v151, v[22:25]
	v_mfma_f32_16x16x4_f32 v[18:21], v139, v151, v[18:21]
	s_add_i32 s10, s8, 11
	s_and_b32 s10, s10, 15
	s_lshl_b32 s64, s10, 6
	v_lshl_add_u64 v[76:77], v[32:33], 0, s[64:65]
	v_lshl_add_u64 v[78:79], v[34:35], 0, s[64:65]
	s_mul_i32 s64, s10, 0xc00
	v_lshl_add_u64 v[80:81], v[36:37], 0, s[64:65]
	global_load_dwordx4 v[132:135], v[76:77], off
	global_load_dwordx4 v[136:139], v[78:79], off
	global_load_dwordx4 v[140:143], v[80:81], off
	global_load_dwordx4 v[144:147], v[80:81], off offset:1024
	global_load_dwordx4 v[148:151], v[80:81], off offset:2048
	s_waitcnt vmcnt(15)
	v_mfma_f32_16x16x4_f32 v[14:17], v56, v88, v[14:17]
	v_mfma_f32_16x16x4_f32 v[6:9], v60, v88, v[6:9]
	v_mfma_f32_16x16x4_f32 v[14:17], v57, v89, v[14:17]
	v_mfma_f32_16x16x4_f32 v[6:9], v61, v89, v[6:9]
	v_mfma_f32_16x16x4_f32 v[14:17], v58, v90, v[14:17]
	v_mfma_f32_16x16x4_f32 v[6:9], v62, v90, v[6:9]
	v_mfma_f32_16x16x4_f32 v[14:17], v59, v91, v[14:17]
	v_mfma_f32_16x16x4_f32 v[6:9], v63, v91, v[6:9]
	v_mfma_f32_16x16x4_f32 v[10:13], v56, v92, v[10:13]
	v_mfma_f32_16x16x4_f32 v[2:5], v60, v92, v[2:5]
	v_mfma_f32_16x16x4_f32 v[10:13], v57, v93, v[10:13]
	v_mfma_f32_16x16x4_f32 v[2:5], v61, v93, v[2:5]
	v_mfma_f32_16x16x4_f32 v[10:13], v58, v94, v[10:13]
	v_mfma_f32_16x16x4_f32 v[2:5], v62, v94, v[2:5]
	v_mfma_f32_16x16x4_f32 v[10:13], v59, v95, v[10:13]
	v_mfma_f32_16x16x4_f32 v[2:5], v63, v95, v[2:5]
	v_mfma_f32_16x16x4_f32 v[22:25], v56, v96, v[22:25]
	v_mfma_f32_16x16x4_f32 v[18:21], v60, v96, v[18:21]
	v_mfma_f32_16x16x4_f32 v[22:25], v57, v97, v[22:25]
	v_mfma_f32_16x16x4_f32 v[18:21], v61, v97, v[18:21]
	v_mfma_f32_16x16x4_f32 v[22:25], v58, v98, v[22:25]
	v_mfma_f32_16x16x4_f32 v[18:21], v62, v98, v[18:21]
	v_mfma_f32_16x16x4_f32 v[22:25], v59, v99, v[22:25]
	v_mfma_f32_16x16x4_f32 v[18:21], v63, v99, v[18:21]
	s_add_i32 s10, s8, 12
	s_and_b32 s10, s10, 15
	s_lshl_b32 s64, s10, 6
	v_lshl_add_u64 v[76:77], v[32:33], 0, s[64:65]
	v_lshl_add_u64 v[78:79], v[34:35], 0, s[64:65]
	s_mul_i32 s64, s10, 0xc00
	v_lshl_add_u64 v[80:81], v[36:37], 0, s[64:65]
	global_load_dwordx4 v[56:59], v[76:77], off
	global_load_dwordx4 v[60:63], v[78:79], off
	global_load_dwordx4 v[88:91], v[80:81], off
	global_load_dwordx4 v[92:95], v[80:81], off offset:1024
	global_load_dwordx4 v[96:99], v[80:81], off offset:2048
	s_waitcnt vmcnt(15)
	v_mfma_f32_16x16x4_f32 v[14:17], v68, v100, v[14:17]
	v_mfma_f32_16x16x4_f32 v[6:9], v72, v100, v[6:9]
	v_mfma_f32_16x16x4_f32 v[14:17], v69, v101, v[14:17]
	v_mfma_f32_16x16x4_f32 v[6:9], v73, v101, v[6:9]
	v_mfma_f32_16x16x4_f32 v[14:17], v70, v102, v[14:17]
	v_mfma_f32_16x16x4_f32 v[6:9], v74, v102, v[6:9]
	v_mfma_f32_16x16x4_f32 v[14:17], v71, v103, v[14:17]
	v_mfma_f32_16x16x4_f32 v[6:9], v75, v103, v[6:9]
	v_mfma_f32_16x16x4_f32 v[10:13], v68, v104, v[10:13]
	v_mfma_f32_16x16x4_f32 v[2:5], v72, v104, v[2:5]
	v_mfma_f32_16x16x4_f32 v[10:13], v69, v105, v[10:13]
	v_mfma_f32_16x16x4_f32 v[2:5], v73, v105, v[2:5]
	v_mfma_f32_16x16x4_f32 v[10:13], v70, v106, v[10:13]
	v_mfma_f32_16x16x4_f32 v[2:5], v74, v106, v[2:5]
	v_mfma_f32_16x16x4_f32 v[10:13], v71, v107, v[10:13]
	v_mfma_f32_16x16x4_f32 v[2:5], v75, v107, v[2:5]
	v_mfma_f32_16x16x4_f32 v[22:25], v68, v108, v[22:25]
	v_mfma_f32_16x16x4_f32 v[18:21], v72, v108, v[18:21]
	v_mfma_f32_16x16x4_f32 v[22:25], v69, v109, v[22:25]
	v_mfma_f32_16x16x4_f32 v[18:21], v73, v109, v[18:21]
	v_mfma_f32_16x16x4_f32 v[22:25], v70, v110, v[22:25]
	v_mfma_f32_16x16x4_f32 v[18:21], v74, v110, v[18:21]
	v_mfma_f32_16x16x4_f32 v[22:25], v71, v111, v[22:25]
	v_mfma_f32_16x16x4_f32 v[18:21], v75, v111, v[18:21]
	s_add_i32 s10, s8, 13
	s_and_b32 s10, s10, 15
	s_lshl_b32 s64, s10, 6
	v_lshl_add_u64 v[76:77], v[32:33], 0, s[64:65]
	v_lshl_add_u64 v[78:79], v[34:35], 0, s[64:65]
	s_mul_i32 s64, s10, 0xc00
	v_lshl_add_u64 v[80:81], v[36:37], 0, s[64:65]
	global_load_dwordx4 v[68:71], v[76:77], off
	global_load_dwordx4 v[72:75], v[78:79], off
	global_load_dwordx4 v[100:103], v[80:81], off
	global_load_dwordx4 v[104:107], v[80:81], off offset:1024
	global_load_dwordx4 v[108:111], v[80:81], off offset:2048
	s_waitcnt vmcnt(15)
	v_mfma_f32_16x16x4_f32 v[14:17], v112, v120, v[14:17]
	v_mfma_f32_16x16x4_f32 v[6:9], v116, v120, v[6:9]
	v_mfma_f32_16x16x4_f32 v[14:17], v113, v121, v[14:17]
	v_mfma_f32_16x16x4_f32 v[6:9], v117, v121, v[6:9]
	v_mfma_f32_16x16x4_f32 v[14:17], v114, v122, v[14:17]
	v_mfma_f32_16x16x4_f32 v[6:9], v118, v122, v[6:9]
	v_mfma_f32_16x16x4_f32 v[14:17], v115, v123, v[14:17]
	v_mfma_f32_16x16x4_f32 v[6:9], v119, v123, v[6:9]
	v_mfma_f32_16x16x4_f32 v[10:13], v112, v124, v[10:13]
	v_mfma_f32_16x16x4_f32 v[2:5], v116, v124, v[2:5]
	v_mfma_f32_16x16x4_f32 v[10:13], v113, v125, v[10:13]
	v_mfma_f32_16x16x4_f32 v[2:5], v117, v125, v[2:5]
	v_mfma_f32_16x16x4_f32 v[10:13], v114, v126, v[10:13]
	v_mfma_f32_16x16x4_f32 v[2:5], v118, v126, v[2:5]
	v_mfma_f32_16x16x4_f32 v[10:13], v115, v127, v[10:13]
	v_mfma_f32_16x16x4_f32 v[2:5], v119, v127, v[2:5]
	v_mfma_f32_16x16x4_f32 v[22:25], v112, v128, v[22:25]
	v_mfma_f32_16x16x4_f32 v[18:21], v116, v128, v[18:21]
	v_mfma_f32_16x16x4_f32 v[22:25], v113, v129, v[22:25]
	v_mfma_f32_16x16x4_f32 v[18:21], v117, v129, v[18:21]
	v_mfma_f32_16x16x4_f32 v[22:25], v114, v130, v[22:25]
	v_mfma_f32_16x16x4_f32 v[18:21], v118, v130, v[18:21]
	v_mfma_f32_16x16x4_f32 v[22:25], v115, v131, v[22:25]
	v_mfma_f32_16x16x4_f32 v[18:21], v119, v131, v[18:21]
	s_add_i32 s10, s8, 14
	s_and_b32 s10, s10, 15
	s_lshl_b32 s64, s10, 6
	v_lshl_add_u64 v[76:77], v[32:33], 0, s[64:65]
	v_lshl_add_u64 v[78:79], v[34:35], 0, s[64:65]
	s_mul_i32 s64, s10, 0xc00
	v_lshl_add_u64 v[80:81], v[36:37], 0, s[64:65]
	global_load_dwordx4 v[112:115], v[76:77], off
	global_load_dwordx4 v[116:119], v[78:79], off
	global_load_dwordx4 v[120:123], v[80:81], off
	global_load_dwordx4 v[124:127], v[80:81], off offset:1024
	global_load_dwordx4 v[128:131], v[80:81], off offset:2048
	s_waitcnt vmcnt(15)
	v_mfma_f32_16x16x4_f32 v[14:17], v132, v140, v[14:17]
	v_mfma_f32_16x16x4_f32 v[6:9], v136, v140, v[6:9]
	v_mfma_f32_16x16x4_f32 v[14:17], v133, v141, v[14:17]
	v_mfma_f32_16x16x4_f32 v[6:9], v137, v141, v[6:9]
	v_mfma_f32_16x16x4_f32 v[14:17], v134, v142, v[14:17]
	v_mfma_f32_16x16x4_f32 v[6:9], v138, v142, v[6:9]
	v_mfma_f32_16x16x4_f32 v[14:17], v135, v143, v[14:17]
	v_mfma_f32_16x16x4_f32 v[6:9], v139, v143, v[6:9]
	v_mfma_f32_16x16x4_f32 v[10:13], v132, v144, v[10:13]
	v_mfma_f32_16x16x4_f32 v[2:5], v136, v144, v[2:5]
	v_mfma_f32_16x16x4_f32 v[10:13], v133, v145, v[10:13]
	v_mfma_f32_16x16x4_f32 v[2:5], v137, v145, v[2:5]
	v_mfma_f32_16x16x4_f32 v[10:13], v134, v146, v[10:13]
	v_mfma_f32_16x16x4_f32 v[2:5], v138, v146, v[2:5]
	v_mfma_f32_16x16x4_f32 v[10:13], v135, v147, v[10:13]
	v_mfma_f32_16x16x4_f32 v[2:5], v139, v147, v[2:5]
	v_mfma_f32_16x16x4_f32 v[22:25], v132, v148, v[22:25]
	v_mfma_f32_16x16x4_f32 v[18:21], v136, v148, v[18:21]
	v_mfma_f32_16x16x4_f32 v[22:25], v133, v149, v[22:25]
	v_mfma_f32_16x16x4_f32 v[18:21], v137, v149, v[18:21]
	v_mfma_f32_16x16x4_f32 v[22:25], v134, v150, v[22:25]
	v_mfma_f32_16x16x4_f32 v[18:21], v138, v150, v[18:21]
	v_mfma_f32_16x16x4_f32 v[22:25], v135, v151, v[22:25]
	v_mfma_f32_16x16x4_f32 v[18:21], v139, v151, v[18:21]
	s_add_i32 s10, s8, 15
	s_and_b32 s10, s10, 15
	s_lshl_b32 s64, s10, 6
	v_lshl_add_u64 v[76:77], v[32:33], 0, s[64:65]
	v_lshl_add_u64 v[78:79], v[34:35], 0, s[64:65]
	s_mul_i32 s64, s10, 0xc00
	v_lshl_add_u64 v[80:81], v[36:37], 0, s[64:65]
	global_load_dwordx4 v[132:135], v[76:77], off
	global_load_dwordx4 v[136:139], v[78:79], off
	global_load_dwordx4 v[140:143], v[80:81], off
	global_load_dwordx4 v[144:147], v[80:81], off offset:1024
	global_load_dwordx4 v[148:151], v[80:81], off offset:2048
	s_waitcnt vmcnt(15)
	v_mfma_f32_16x16x4_f32 v[14:17], v56, v88, v[14:17]
	v_mfma_f32_16x16x4_f32 v[6:9], v60, v88, v[6:9]
	v_mfma_f32_16x16x4_f32 v[14:17], v57, v89, v[14:17]
	v_mfma_f32_16x16x4_f32 v[6:9], v61, v89, v[6:9]
	v_mfma_f32_16x16x4_f32 v[14:17], v58, v90, v[14:17]
	v_mfma_f32_16x16x4_f32 v[6:9], v62, v90, v[6:9]
	v_mfma_f32_16x16x4_f32 v[14:17], v59, v91, v[14:17]
	v_mfma_f32_16x16x4_f32 v[6:9], v63, v91, v[6:9]
	v_mfma_f32_16x16x4_f32 v[10:13], v56, v92, v[10:13]
	v_mfma_f32_16x16x4_f32 v[2:5], v60, v92, v[2:5]
	v_mfma_f32_16x16x4_f32 v[10:13], v57, v93, v[10:13]
	v_mfma_f32_16x16x4_f32 v[2:5], v61, v93, v[2:5]
	v_mfma_f32_16x16x4_f32 v[10:13], v58, v94, v[10:13]
	v_mfma_f32_16x16x4_f32 v[2:5], v62, v94, v[2:5]
	v_mfma_f32_16x16x4_f32 v[10:13], v59, v95, v[10:13]
	v_mfma_f32_16x16x4_f32 v[2:5], v63, v95, v[2:5]
	v_mfma_f32_16x16x4_f32 v[22:25], v56, v96, v[22:25]
	v_mfma_f32_16x16x4_f32 v[18:21], v60, v96, v[18:21]
	v_mfma_f32_16x16x4_f32 v[22:25], v57, v97, v[22:25]
	v_mfma_f32_16x16x4_f32 v[18:21], v61, v97, v[18:21]
	v_mfma_f32_16x16x4_f32 v[22:25], v58, v98, v[22:25]
	v_mfma_f32_16x16x4_f32 v[18:21], v62, v98, v[18:21]
	v_mfma_f32_16x16x4_f32 v[22:25], v59, v99, v[22:25]
	v_mfma_f32_16x16x4_f32 v[18:21], v63, v99, v[18:21]
	s_waitcnt vmcnt(10)
	v_mfma_f32_16x16x4_f32 v[14:17], v68, v100, v[14:17]
	v_mfma_f32_16x16x4_f32 v[6:9], v72, v100, v[6:9]
	v_mfma_f32_16x16x4_f32 v[14:17], v69, v101, v[14:17]
	v_mfma_f32_16x16x4_f32 v[6:9], v73, v101, v[6:9]
	v_mfma_f32_16x16x4_f32 v[14:17], v70, v102, v[14:17]
	v_mfma_f32_16x16x4_f32 v[6:9], v74, v102, v[6:9]
	v_mfma_f32_16x16x4_f32 v[14:17], v71, v103, v[14:17]
	v_mfma_f32_16x16x4_f32 v[6:9], v75, v103, v[6:9]
	v_mfma_f32_16x16x4_f32 v[10:13], v68, v104, v[10:13]
	v_mfma_f32_16x16x4_f32 v[2:5], v72, v104, v[2:5]
	v_mfma_f32_16x16x4_f32 v[10:13], v69, v105, v[10:13]
	v_mfma_f32_16x16x4_f32 v[2:5], v73, v105, v[2:5]
	v_mfma_f32_16x16x4_f32 v[10:13], v70, v106, v[10:13]
	v_mfma_f32_16x16x4_f32 v[2:5], v74, v106, v[2:5]
	v_mfma_f32_16x16x4_f32 v[10:13], v71, v107, v[10:13]
	v_mfma_f32_16x16x4_f32 v[2:5], v75, v107, v[2:5]
	v_mfma_f32_16x16x4_f32 v[22:25], v68, v108, v[22:25]
	v_mfma_f32_16x16x4_f32 v[18:21], v72, v108, v[18:21]
	v_mfma_f32_16x16x4_f32 v[22:25], v69, v109, v[22:25]
	v_mfma_f32_16x16x4_f32 v[18:21], v73, v109, v[18:21]
	v_mfma_f32_16x16x4_f32 v[22:25], v70, v110, v[22:25]
	v_mfma_f32_16x16x4_f32 v[18:21], v74, v110, v[18:21]
	v_mfma_f32_16x16x4_f32 v[22:25], v71, v111, v[22:25]
	v_mfma_f32_16x16x4_f32 v[18:21], v75, v111, v[18:21]
	s_waitcnt vmcnt(5)
	v_mfma_f32_16x16x4_f32 v[14:17], v112, v120, v[14:17]
	v_mfma_f32_16x16x4_f32 v[6:9], v116, v120, v[6:9]
	v_mfma_f32_16x16x4_f32 v[14:17], v113, v121, v[14:17]
	v_mfma_f32_16x16x4_f32 v[6:9], v117, v121, v[6:9]
	v_mfma_f32_16x16x4_f32 v[14:17], v114, v122, v[14:17]
	v_mfma_f32_16x16x4_f32 v[6:9], v118, v122, v[6:9]
	v_mfma_f32_16x16x4_f32 v[14:17], v115, v123, v[14:17]
	v_mfma_f32_16x16x4_f32 v[6:9], v119, v123, v[6:9]
	v_mfma_f32_16x16x4_f32 v[10:13], v112, v124, v[10:13]
	v_mfma_f32_16x16x4_f32 v[2:5], v116, v124, v[2:5]
	v_mfma_f32_16x16x4_f32 v[10:13], v113, v125, v[10:13]
	v_mfma_f32_16x16x4_f32 v[2:5], v117, v125, v[2:5]
	v_mfma_f32_16x16x4_f32 v[10:13], v114, v126, v[10:13]
	v_mfma_f32_16x16x4_f32 v[2:5], v118, v126, v[2:5]
	v_mfma_f32_16x16x4_f32 v[10:13], v115, v127, v[10:13]
	v_mfma_f32_16x16x4_f32 v[2:5], v119, v127, v[2:5]
	v_mfma_f32_16x16x4_f32 v[22:25], v112, v128, v[22:25]
	v_mfma_f32_16x16x4_f32 v[18:21], v116, v128, v[18:21]
	v_mfma_f32_16x16x4_f32 v[22:25], v113, v129, v[22:25]
	v_mfma_f32_16x16x4_f32 v[18:21], v117, v129, v[18:21]
	v_mfma_f32_16x16x4_f32 v[22:25], v114, v130, v[22:25]
	v_mfma_f32_16x16x4_f32 v[18:21], v118, v130, v[18:21]
	v_mfma_f32_16x16x4_f32 v[22:25], v115, v131, v[22:25]
	v_mfma_f32_16x16x4_f32 v[18:21], v119, v131, v[18:21]
	s_waitcnt vmcnt(0)
	v_mfma_f32_16x16x4_f32 v[14:17], v132, v140, v[14:17]
	v_mfma_f32_16x16x4_f32 v[6:9], v136, v140, v[6:9]
	v_mfma_f32_16x16x4_f32 v[14:17], v133, v141, v[14:17]
	v_mfma_f32_16x16x4_f32 v[6:9], v137, v141, v[6:9]
	v_mfma_f32_16x16x4_f32 v[14:17], v134, v142, v[14:17]
	v_mfma_f32_16x16x4_f32 v[6:9], v138, v142, v[6:9]
	v_mfma_f32_16x16x4_f32 v[14:17], v135, v143, v[14:17]
	v_mfma_f32_16x16x4_f32 v[6:9], v139, v143, v[6:9]
	v_mfma_f32_16x16x4_f32 v[10:13], v132, v144, v[10:13]
	v_mfma_f32_16x16x4_f32 v[2:5], v136, v144, v[2:5]
	v_mfma_f32_16x16x4_f32 v[10:13], v133, v145, v[10:13]
	v_mfma_f32_16x16x4_f32 v[2:5], v137, v145, v[2:5]
	v_mfma_f32_16x16x4_f32 v[10:13], v134, v146, v[10:13]
	v_mfma_f32_16x16x4_f32 v[2:5], v138, v146, v[2:5]
	v_mfma_f32_16x16x4_f32 v[10:13], v135, v147, v[10:13]
	v_mfma_f32_16x16x4_f32 v[2:5], v139, v147, v[2:5]
	v_mfma_f32_16x16x4_f32 v[22:25], v132, v148, v[22:25]
	v_mfma_f32_16x16x4_f32 v[18:21], v136, v148, v[18:21]
	v_mfma_f32_16x16x4_f32 v[22:25], v133, v149, v[22:25]
	v_mfma_f32_16x16x4_f32 v[18:21], v137, v149, v[18:21]
	v_mfma_f32_16x16x4_f32 v[22:25], v134, v150, v[22:25]
	v_mfma_f32_16x16x4_f32 v[18:21], v138, v150, v[18:21]
	v_mfma_f32_16x16x4_f32 v[22:25], v135, v151, v[22:25]
	v_mfma_f32_16x16x4_f32 v[18:21], v139, v151, v[18:21]


	s_setprio 0
	ds_write2_b32 v40, v14, v10 offset1:16
	ds_write2_b32 v40, v16, v12 offset0:96 offset1:112
	s_nop 4
	ds_write2_b32 v40, v22, v15 offset0:32 offset1:48
	ds_write2_b32 v40, v11, v23 offset0:64 offset1:80
	ds_write2_b32 v40, v24, v17 offset0:128 offset1:144
	ds_write2_b32 v40, v13, v25 offset0:160 offset1:176
	v_add_u32_e32 v10, 0xc00, v40
	ds_write2_b32 v10, v6, v2 offset1:16
	ds_write2_b32 v10, v8, v4 offset0:96 offset1:112
	ds_write2_b32 v10, v18, v7 offset0:32 offset1:48
	ds_write2_b32 v10, v3, v19 offset0:64 offset1:80
	ds_write2_b32 v10, v20, v9 offset0:128 offset1:144
	ds_write2_b32 v10, v5, v21 offset0:160 offset1:176
	s_waitcnt lgkmcnt(0)
	s_barrier
	s_and_saveexec_b64 s[8:9], s[6:7]
	s_cbranch_execz .LBB0_3241
	s_mov_b64 s[10:11], 0
	v_mov_b32_e32 v2, v39
	v_mov_b32_e32 v3, v66
